# speedup vs baseline: 1.0076x; 1.0013x over previous
_Z2kBPKfPKDv4_jPKDF16_S0_S0_S0_Pf:
	v_lshrrev_b32_e32 v11, 7, v0
	s_load_dwordx8 s[4:11], s[0:1], 0x0
	v_readfirstlane_b32 s12, v0
	s_cmpk_lt_u32 s12, 0x100
	s_cbranch_scc1 .LkB_noprio
	s_setprio 1
.LkB_noprio:
	v_lshl_or_b32 v2, s2, 2, v11
	s_mov_b32 s2, 0x4ec4ec4f
	v_mul_hi_i32 v1, v2, s2
	v_lshrrev_b32_e32 v3, 31, v1
	v_ashrrev_i32_e32 v1, 2, v1
	v_add_u32_e32 v1, v1, v3
	v_and_b32_e32 v108, 15, v0
	v_mad_u64_u32 v[4:5], s[2:3], v1, -13, v[2:3]
	v_lshlrev_b32_e32 v102, 4, v0
	v_mov_b32_e32 v103, 0
	v_lshl_or_b32 v10, v4, 4, v108
	s_waitcnt lgkmcnt(0)
	v_lshl_add_u64 v[4:5], s[8:9], 0, v[102:103]
	s_movk_i32 s2, 0x2000
	v_add_co_u32_e32 v6, vcc, s2, v4
	s_movk_i32 s2, 0x4000
	s_nop 0
	v_addc_co_u32_e32 v7, vcc, 0, v5, vcc
	v_add_co_u32_e32 v8, vcc, s2, v4
	s_movk_i32 s2, 0x6000
	s_nop 0
	v_addc_co_u32_e32 v9, vcc, 0, v5, vcc
	global_load_dwordx4 v[14:17], v102, s[8:9]
	global_load_dwordx4 v[18:21], v[6:7], off
	global_load_dwordx4 v[22:25], v[8:9], off
	v_add_co_u32_e32 v6, vcc, s2, v4
	s_mov_b32 s2, 0x8000
	s_nop 0
	v_addc_co_u32_e32 v7, vcc, 0, v5, vcc
	v_add_co_u32_e32 v8, vcc, s2, v4
	s_mov_b32 s2, 0xa000
	s_nop 0
	v_addc_co_u32_e32 v9, vcc, 0, v5, vcc
	global_load_dwordx4 v[26:29], v[6:7], off
	global_load_dwordx4 v[30:33], v[8:9], off
	v_add_co_u32_e32 v6, vcc, s2, v4
	s_mov_b32 s2, 0xc000
	s_nop 0
	v_addc_co_u32_e32 v7, vcc, 0, v5, vcc
	v_add_co_u32_e32 v8, vcc, s2, v4
	s_mov_b32 s2, 0xe000
	s_nop 0
	v_addc_co_u32_e32 v9, vcc, 0, v5, vcc
	v_add_co_u32_e32 v4, vcc, s2, v4
	s_movk_i32 s2, 0xc8
	s_nop 0
	v_addc_co_u32_e32 v5, vcc, 0, v5, vcc
	global_load_dwordx4 v[34:37], v[6:7], off
	global_load_dwordx4 v[38:41], v[8:9], off
	v_mov_b32_e32 v3, 0xc7
	v_cmp_gt_i32_e32 vcc, s2, v10
	global_load_dwordx4 v[42:45], v[4:5], off
	s_movk_i32 s2, 0x320
	v_cndmask_b32_e32 v4, v3, v10, vcc
	v_mad_u64_u32 v[4:5], s[2:3], v1, s2, v[4:5]
	v_and_b32_e32 v6, 48, v0
	v_mov_b32_e32 v7, v103
	v_ashrrev_i32_e32 v5, 31, v4
	v_lshl_add_u64 v[8:9], s[4:5], 0, v[6:7]
	v_lshlrev_b64 v[12:13], 6, v[4:5]
	v_lshl_add_u64 v[12:13], v[8:9], 0, v[12:13]
	global_load_dwordx4 v[46:49], v[12:13], off
	v_add_u32_e32 v12, 0xc8, v4
	v_ashrrev_i32_e32 v13, 31, v12
	v_lshlrev_b64 v[12:13], 6, v[12:13]
	v_lshl_add_u64 v[12:13], v[8:9], 0, v[12:13]
	global_load_dwordx4 v[50:53], v[12:13], off
	v_add_u32_e32 v12, 0x190, v4
	v_ashrrev_i32_e32 v13, 31, v12
	v_lshlrev_b64 v[12:13], 6, v[12:13]
	v_lshl_add_u64 v[12:13], v[8:9], 0, v[12:13]
	global_load_dwordx4 v[54:57], v[12:13], off
	v_add_u32_e32 v4, 0x258, v4
	v_ashrrev_i32_e32 v5, 31, v4
	v_lshlrev_b64 v[4:5], 6, v[4:5]
	v_lshl_add_u64 v[4:5], v[8:9], 0, v[4:5]
	global_load_dwordx4 v[58:61], v[4:5], off
	v_and_b32_e32 v13, 63, v0
	v_lshl_or_b32 v2, v2, 8, v13
	v_ashrrev_i32_e32 v3, 31, v2
	v_lshl_add_u64 v[2:3], v[2:3], 4, s[6:7]
	global_load_dwordx4 v[62:65], v[2:3], off
	global_load_dwordx4 v[66:69], v[2:3], off offset:1024
	global_load_dwordx4 v[70:73], v[2:3], off offset:2048
	global_load_dwordx4 v[74:77], v[2:3], off offset:3072
	s_load_dwordx4 s[4:7], s[0:1], 0x20
	v_bfe_u32 v12, v0, 6, 1
	v_lshl_add_u64 v[2:3], s[10:11], 0, v[6:7]
	v_and_b32_e32 v0, 64, v0
	v_cmp_gt_u32_e64 s[2:3], 16, v13
	s_waitcnt lgkmcnt(0)
	v_lshl_add_u64 v[4:5], s[4:5], 0, v[6:7]
	v_lshlrev_b32_e32 v6, 8, v12
	v_lshl_add_u64 v[104:105], v[2:3], 0, v[6:7]
	v_lshl_add_u64 v[106:107], v[4:5], 0, v[6:7]
	global_load_dwordx4 v[78:81], v[104:105], off
	global_load_dwordx4 v[82:85], v[104:105], off offset:64
	global_load_dwordx4 v[86:89], v[106:107], off
	global_load_dwordx4 v[90:93], v[106:107], off offset:64
	global_load_dwordx4 v[94:97], v[104:105], off offset:128
	global_load_dwordx4 v[6:9], v[104:105], off offset:192
	global_load_dwordx4 v[98:101], v[106:107], off offset:128
	global_load_dwordx4 v[2:5], v[106:107], off offset:192
	s_load_dword s6, s[6:7], 0x0
	s_waitcnt vmcnt(23)
	ds_write_b128 v102, v[14:17]
	s_waitcnt vmcnt(22)
	ds_write_b128 v102, v[18:21] offset:8192
	s_waitcnt vmcnt(21)
	ds_write_b128 v102, v[22:25] offset:16384
	s_waitcnt vmcnt(20)
	ds_write_b128 v102, v[26:29] offset:24576
	s_waitcnt vmcnt(19)
	ds_write_b128 v102, v[30:33] offset:32768
	s_waitcnt vmcnt(18)
	ds_write_b128 v102, v[34:37] offset:40960
	s_waitcnt vmcnt(17)
	ds_write_b128 v102, v[38:41] offset:49152
	s_waitcnt vmcnt(16)
	ds_write_b128 v102, v[42:45] offset:57344
	v_lshlrev_b32_e32 v14, 15, v12
	v_lshl_or_b32 v38, v13, 4, v14
	s_waitcnt lgkmcnt(0)
	s_barrier
	ds_read_b128 v[14:17], v38
	ds_read_b128 v[18:21], v38 offset:1024
	s_waitcnt vmcnt(15) lgkmcnt(1)
	v_mfma_f32_16x16x32_f16 v[14:17], v[14:17], v[46:49], 0
	ds_read_b128 v[22:25], v38 offset:2048
	ds_read_b128 v[26:29], v38 offset:10240
	ds_read_b128 v[30:33], v38 offset:18432
	s_waitcnt vmcnt(14) lgkmcnt(3)
	v_mfma_f32_16x16x32_f16 v[14:17], v[18:21], v[50:53], v[14:17]
	ds_read_b128 v[18:21], v38 offset:3072
	ds_read_b128 v[34:37], v38 offset:26624
	v_cmp_ne_u32_e64 s[4:5], 0, v0
	s_waitcnt vmcnt(13) lgkmcnt(4)
	v_mfma_f32_16x16x32_f16 v[14:17], v[22:25], v[54:57], v[14:17]
	ds_read_b128 v[22:25], v38 offset:4096
	s_and_b64 s[8:9], s[4:5], s[2:3]
	v_lshlrev_b32_e32 v0, 2, v108
	s_waitcnt vmcnt(12) lgkmcnt(2)
	v_mfma_f32_16x16x32_f16 v[14:17], v[18:21], v[58:61], v[14:17]
	ds_read_b128 v[18:21], v38 offset:5120
	s_waitcnt vmcnt(11) lgkmcnt(1)
	v_mfma_f32_16x16x32_f16 v[14:17], v[22:25], v[62:65], v[14:17]
	ds_read_b128 v[22:25], v38 offset:6144
	s_waitcnt vmcnt(10) lgkmcnt(1)
	v_mfma_f32_16x16x32_f16 v[14:17], v[18:21], v[66:69], v[14:17]
	ds_read_b128 v[18:21], v38 offset:7168
	s_waitcnt vmcnt(9) lgkmcnt(1)
	v_mfma_f32_16x16x32_f16 v[14:17], v[22:25], v[70:73], v[14:17]
	ds_read_b128 v[22:25], v38 offset:8192
	s_waitcnt vmcnt(8) lgkmcnt(1)
	v_mfma_f32_16x16x32_f16 v[14:17], v[18:21], v[74:77], v[14:17]
	ds_read_b128 v[18:21], v38 offset:9216
	s_waitcnt lgkmcnt(1)
	v_mfma_f32_16x16x32_f16 v[22:25], v[22:25], v[46:49], 0
	s_waitcnt vmcnt(7)
	s_nop 3
	v_add_f32_e32 v14, v14, v78
	v_mul_f32_e32 v14, 0x4038aa3b, v14
	v_add_f32_e32 v15, v15, v79
	s_waitcnt lgkmcnt(0)
	v_mfma_f32_16x16x32_f16 v[18:21], v[18:21], v[50:53], v[22:25]
	v_exp_f32_e32 v14, v14
	v_mul_f32_e32 v15, 0x4038aa3b, v15
	s_nop 0
	ds_read_b128 v[22:25], v38 offset:11264
	v_mfma_f32_16x16x32_f16 v[18:21], v[26:29], v[54:57], v[18:21]
	ds_read_b128 v[26:29], v38 offset:12288
	v_add_f32_e32 v16, v16, v80
	v_exp_f32_e32 v15, v15
	s_waitcnt lgkmcnt(1)
	v_mfma_f32_16x16x32_f16 v[18:21], v[22:25], v[58:61], v[18:21]
	ds_read_b128 v[22:25], v38 offset:13312
	v_mul_f32_e32 v16, 0x4038aa3b, v16
	v_add_f32_e32 v17, v17, v81
	s_waitcnt lgkmcnt(1)
	v_mfma_f32_16x16x32_f16 v[18:21], v[26:29], v[62:65], v[18:21]
	ds_read_b128 v[26:29], v38 offset:14336
	v_exp_f32_e32 v16, v16
	v_mul_f32_e32 v17, 0x4038aa3b, v17
	s_waitcnt lgkmcnt(1)
	v_mfma_f32_16x16x32_f16 v[18:21], v[22:25], v[66:69], v[18:21]
	ds_read_b128 v[22:25], v38 offset:15360
	v_exp_f32_e32 v17, v17
	v_add_f32_e32 v14, 1.0, v14
	s_waitcnt lgkmcnt(1)
	v_mfma_f32_16x16x32_f16 v[18:21], v[26:29], v[70:73], v[18:21]
	ds_read_b128 v[26:29], v38 offset:16384
	v_rcp_f32_e32 v14, v14
	v_add_f32_e32 v15, 1.0, v15
	s_waitcnt lgkmcnt(1)
	v_mfma_f32_16x16x32_f16 v[18:21], v[22:25], v[74:77], v[18:21]
	ds_read_b128 v[22:25], v38 offset:17408
	v_rcp_f32_e32 v15, v15
	v_add_f32_e32 v16, 1.0, v16
	s_waitcnt lgkmcnt(1)
	v_mfma_f32_16x16x32_f16 v[26:29], v[26:29], v[46:49], 0
	v_rcp_f32_e32 v16, v16
	v_add_f32_e32 v17, 1.0, v17
	v_rcp_f32_e32 v17, v17
	s_waitcnt lgkmcnt(0)
	v_mfma_f32_16x16x32_f16 v[22:25], v[22:25], v[50:53], v[26:29]
	v_fma_f32 v14, v14, -2.0, 1.0
	s_nop 1
	ds_read_b128 v[26:29], v38 offset:19456
	s_waitcnt vmcnt(5)
	v_fma_f32 v14, v14, v86, 0
	v_mfma_f32_16x16x32_f16 v[22:25], v[30:33], v[54:57], v[22:25]
	ds_read_b128 v[30:33], v38 offset:20480
	v_fma_f32 v15, v15, -2.0, 1.0
	v_fmac_f32_e32 v14, v15, v87
	s_waitcnt lgkmcnt(1)
	v_mfma_f32_16x16x32_f16 v[22:25], v[26:29], v[58:61], v[22:25]
	ds_read_b128 v[26:29], v38 offset:21504
	v_fma_f32 v15, v16, -2.0, 1.0
	v_fmac_f32_e32 v14, v15, v88
	s_waitcnt lgkmcnt(1)
	v_mfma_f32_16x16x32_f16 v[22:25], v[30:33], v[62:65], v[22:25]
	ds_read_b128 v[30:33], v38 offset:22528
	v_fma_f32 v15, v17, -2.0, 1.0
	v_add_f32_e32 v16, v18, v82
	s_waitcnt lgkmcnt(1)
	v_mfma_f32_16x16x32_f16 v[22:25], v[26:29], v[66:69], v[22:25]
	ds_read_b128 v[26:29], v38 offset:23552
	v_add_f32_e32 v17, v19, v83
	v_mul_f32_e32 v16, 0x4038aa3b, v16
	s_waitcnt lgkmcnt(1)
	v_mfma_f32_16x16x32_f16 v[22:25], v[30:33], v[70:73], v[22:25]
	ds_read_b128 v[30:33], v38 offset:24576
	v_mul_f32_e32 v17, 0x4038aa3b, v17
	v_exp_f32_e32 v16, v16
	s_waitcnt lgkmcnt(1)
	v_mfma_f32_16x16x32_f16 v[22:25], v[26:29], v[74:77], v[22:25]
	ds_read_b128 v[26:29], v38 offset:25600
	v_exp_f32_e32 v17, v17
	v_fmac_f32_e32 v14, v15, v89
	s_waitcnt lgkmcnt(1)
	v_mfma_f32_16x16x32_f16 v[30:33], v[30:33], v[46:49], 0
	v_add_f32_e32 v15, 1.0, v16
	v_add_f32_e32 v16, 1.0, v17
	v_add_f32_e32 v17, v20, v84
	s_waitcnt lgkmcnt(0)
	v_mfma_f32_16x16x32_f16 v[26:29], v[26:29], v[50:53], v[30:33]
	v_rcp_f32_e32 v15, v15
	s_nop 1
	ds_read_b128 v[30:33], v38 offset:27648
	v_mul_f32_e32 v17, 0x4038aa3b, v17
	v_mfma_f32_16x16x32_f16 v[26:29], v[34:37], v[54:57], v[26:29]
	ds_read_b128 v[34:37], v38 offset:28672
	v_rcp_f32_e32 v16, v16
	v_exp_f32_e32 v17, v17
	s_waitcnt lgkmcnt(1)
	v_mfma_f32_16x16x32_f16 v[26:29], v[30:33], v[58:61], v[26:29]
	ds_read_b128 v[30:33], v38 offset:29696
	v_fma_f32 v15, v15, -2.0, 1.0
	s_waitcnt vmcnt(4)
	v_fmac_f32_e32 v14, v15, v90
	v_fma_f32 v15, v16, -2.0, 1.0
	v_add_f32_e32 v16, 1.0, v17
	v_add_f32_e32 v17, v21, v85
	s_waitcnt lgkmcnt(1)
	v_mfma_f32_16x16x32_f16 v[26:29], v[34:37], v[62:65], v[26:29]
	ds_read_b128 v[34:37], v38 offset:30720
	v_rcp_f32_e32 v16, v16
	v_mul_f32_e32 v17, 0x4038aa3b, v17
	v_exp_f32_e32 v17, v17
	s_waitcnt lgkmcnt(1)
	v_mfma_f32_16x16x32_f16 v[26:29], v[30:33], v[66:69], v[26:29]
	ds_read_b128 v[30:33], v38 offset:31744
	v_fmac_f32_e32 v14, v15, v91
	v_fma_f32 v15, v16, -2.0, 1.0
	s_waitcnt vmcnt(3)
	v_add_f32_e32 v16, v22, v94
	v_fmac_f32_e32 v14, v15, v92
	v_add_f32_e32 v15, 1.0, v17
	v_mul_f32_e32 v16, 0x4038aa3b, v16
	v_add_f32_e32 v17, v23, v95
	v_exp_f32_e32 v16, v16
	v_mul_f32_e32 v17, 0x4038aa3b, v17
	v_exp_f32_e32 v17, v17
	s_waitcnt lgkmcnt(1)
	v_mfma_f32_16x16x32_f16 v[26:29], v[34:37], v[70:73], v[26:29]
	v_rcp_f32_e32 v15, v15
	v_add_f32_e32 v16, 1.0, v16
	v_rcp_f32_e32 v16, v16
	v_add_f32_e32 v17, 1.0, v17
	v_rcp_f32_e32 v17, v17
	s_waitcnt lgkmcnt(0)
	v_mfma_f32_16x16x32_f16 v[26:29], v[30:33], v[74:77], v[26:29]
	v_fma_f32 v15, v15, -2.0, 1.0
	v_fmac_f32_e32 v14, v15, v93
	v_fma_f32 v15, v16, -2.0, 1.0
	v_add_f32_e32 v16, v24, v96
	s_waitcnt vmcnt(1)
	v_fmac_f32_e32 v14, v15, v98
	v_fma_f32 v15, v17, -2.0, 1.0
	v_mul_f32_e32 v16, 0x4038aa3b, v16
	v_add_f32_e32 v17, v25, v97
	v_exp_f32_e32 v16, v16
	v_mul_f32_e32 v17, 0x4038aa3b, v17
	v_add_f32_e32 v6, v26, v6
	v_exp_f32_e32 v17, v17
	v_mul_f32_e32 v6, 0x4038aa3b, v6
	v_exp_f32_e32 v6, v6
	v_fmac_f32_e32 v14, v15, v99
	v_add_f32_e32 v15, 1.0, v16
	v_rcp_f32_e32 v15, v15
	v_add_f32_e32 v16, 1.0, v17
	v_rcp_f32_e32 v16, v16
	v_add_f32_e32 v6, 1.0, v6
	v_rcp_f32_e32 v6, v6
	v_add_f32_e32 v7, v27, v7
	v_mul_f32_e32 v7, 0x4038aa3b, v7
	v_fma_f32 v15, v15, -2.0, 1.0
	v_exp_f32_e32 v7, v7
	v_fmac_f32_e32 v14, v15, v100
	v_fma_f32 v15, v16, -2.0, 1.0
	v_fmac_f32_e32 v14, v15, v101
	v_fma_f32 v6, v6, -2.0, 1.0
	s_waitcnt vmcnt(0)
	v_fmac_f32_e32 v14, v6, v2
	v_add_f32_e32 v6, v28, v8
	v_add_f32_e32 v2, 1.0, v7
	v_mul_f32_e32 v6, 0x4038aa3b, v6
	v_add_f32_e32 v7, v29, v9
	v_exp_f32_e32 v6, v6
	v_mul_f32_e32 v7, 0x4038aa3b, v7
	v_exp_f32_e32 v7, v7
	v_rcp_f32_e32 v2, v2
	v_add_f32_e32 v6, 1.0, v6
	v_rcp_f32_e32 v6, v6
	v_add_f32_e32 v7, 1.0, v7
	v_rcp_f32_e32 v7, v7
	v_fma_f32 v2, v2, -2.0, 1.0
	v_fmac_f32_e32 v14, v2, v3
	v_fma_f32 v2, v6, -2.0, 1.0
	v_fmac_f32_e32 v14, v2, v4
	v_fma_f32 v2, v7, -2.0, 1.0
	v_fmac_f32_e32 v14, v2, v5
	v_mov_b32_e32 v2, v14
	s_nop 1
	v_permlane16_swap_b32_e32 v14, v2
	v_add_f32_e32 v2, v14, v2
	v_mov_b32_e32 v3, v2
	s_nop 1
	v_permlane32_swap_b32_e32 v2, v3
	v_add_f32_e32 v2, v2, v3
	s_and_saveexec_b64 s[4:5], s[8:9]
	v_lshl_or_b32 v3, v11, 6, v0
	v_add_u32_e32 v3, 0x10000, v3
	ds_write_b32 v3, v2
	s_or_b64 exec, exec, s[4:5]
	v_cmp_eq_u32_e64 s[4:5], 0, v12
	s_and_b64 s[2:3], s[4:5], s[2:3]
	s_and_b64 s[2:3], s[2:3], vcc
	s_waitcnt lgkmcnt(0)
	s_barrier
	s_and_saveexec_b64 s[4:5], s[2:3]
	s_cbranch_execz .LBB1_4
	v_lshl_or_b32 v0, v11, 6, v0
	v_add_u32_e32 v0, 0x10000, v0
	ds_read_b32 v0, v0
	s_load_dwordx2 s[0:1], s[0:1], 0x30
	s_movk_i32 s2, 0xc8
	s_waitcnt lgkmcnt(0)
	v_add_f32_e32 v0, v2, v0
	v_add_f32_e32 v0, s6, v0
	v_mul_f32_e32 v0, 0xbfb8aa3b, v0
	v_exp_f32_e32 v0, v0
	s_nop 0
	v_add_f32_e32 v0, 1.0, v0
	v_rcp_f32_e32 v2, v0
	v_mad_u64_u32 v[0:1], s[2:3], v1, s2, v[10:11]
	v_ashrrev_i32_e32 v1, 31, v0
	v_lshl_add_u64 v[0:1], v[0:1], 2, s[0:1]
	global_store_dword v[0:1], v2, off
